# v9 + pipelined mlstate DN tail, padded so later code shifts by exactly 2048 B
# speedup vs baseline: 1.0053x; 1.0006x over previous
.LBB0_742:
	s_or_b64 exec, exec, s[0:1]
	v_lshl_add_u64 v[10:11], v[36:37], 0, s[20:21]
	v_lshlrev_b64 v[10:11], 2, v[10:11]
	v_lshl_add_u64 v[14:15], s[18:19], 0, v[10:11]
	s_movk_i32 s0, 0x1000
	v_add_co_u32_e32 v12, vcc, s0, v14
	global_load_dwordx4 v[92:95], v[14:15], off offset:3072
	global_load_dwordx4 v[96:99], v[14:15], off offset:3088
	global_load_dwordx4 v[100:103], v[14:15], off offset:1024
	global_load_dwordx4 v[104:107], v[14:15], off offset:1040
	v_addc_co_u32_e32 v13, vcc, 0, v15, vcc
	global_load_dwordx4 v[108:111], v[12:13], off offset:1024
	s_mov_b64 s[38:39], 0x1400
	v_lshl_add_u64 v[16:17], v[14:15], 0, s[38:39]
	v_lshl_add_u64 v[22:23], s[12:13], 0, v[10:11]
	global_load_dwordx4 v[112:115], v[16:17], off offset:16
	global_load_dwordx4 v[116:119], v[22:23], off offset:1024
	global_load_dwordx4 v[120:123], v[22:23], off offset:1040
	s_waitcnt vmcnt(8)
	v_and_b32_e32 v91, 0xffff0000, v9
	v_lshlrev_b32_e32 v124, 16, v9
	v_and_b32_e32 v125, 0xffff0000, v8
	v_lshlrev_b32_e32 v126, 16, v8
	v_and_b32_e32 v127, 0xffff0000, v7
	v_lshlrev_b32_e32 v128, 16, v7
	v_and_b32_e32 v129, 0xffff0000, v6
	v_lshlrev_b32_e32 v130, 16, v6
	v_and_b32_e32 v131, 0xffff0000, v5
	v_lshlrev_b32_e32 v132, 16, v5
	v_and_b32_e32 v133, 0xffff0000, v4
	v_lshlrev_b32_e32 v134, 16, v4
	v_and_b32_e32 v135, 0xffff0000, v3
	v_lshlrev_b32_e32 v136, 16, v3
	v_and_b32_e32 v137, 0xffff0000, v2
	v_lshlrev_b32_e32 v138, 16, v2
	global_load_dwordx4 v[2:5], v[14:15], off offset:1072
	global_load_dwordx4 v[18:21], v[14:15], off offset:1056
	global_load_dwordx4 v[10:13], v[14:15], off offset:3120
	global_load_dwordx4 v[26:29], v[14:15], off offset:3104
	global_load_dwordx4 v[6:9], v[22:23], off offset:1072
	s_nop 0
	global_load_dwordx4 v[22:25], v[22:23], off offset:1056
	s_nop 0
	global_load_dwordx4 v[30:33], v[16:17], off offset:32
	s_nop 0
	global_load_dwordx4 v[14:17], v[16:17], off offset:48
	s_lshl_b32 s20, s20, 1
	v_lshl_add_u64 v[50:51], v[50:51], 0, s[20:21]
	v_lshl_add_u64 v[50:51], v[36:37], 1, v[50:51]
	s_ashr_i32 s4, s10, 31
	s_waitcnt vmcnt(15)
	v_mul_f32_e32 v95, v95, v135
	v_mul_f32_e32 v92, v92, v138
	s_waitcnt vmcnt(13)
	v_fmac_f32_e32 v95, v79, v103
	v_mul_f32_e32 v93, v93, v137
	v_mul_f32_e32 v94, v94, v136
	v_fmac_f32_e32 v92, v76, v100
	s_waitcnt vmcnt(11)
	v_fmac_f32_e32 v95, v88, v111
	v_mul_f32_e32 v96, v96, v134
	v_fmac_f32_e32 v93, v77, v101
	v_fmac_f32_e32 v94, v78, v102
	v_fmac_f32_e32 v92, v75, v108
	s_waitcnt vmcnt(9)
	v_add_f32_e32 v78, v119, v95
	v_mul_f32_e32 v97, v97, v133
	v_fmac_f32_e32 v96, v80, v104
	v_fmac_f32_e32 v93, v86, v109
	v_fmac_f32_e32 v94, v87, v110
	v_add_f32_e32 v75, v116, v92
	v_mul_f32_e32 v87, 0xbfb8aa3b, v78
	v_mul_f32_e32 v98, v98, v132
	v_fmac_f32_e32 v97, v81, v105
	v_fmac_f32_e32 v96, v89, v112
	v_add_f32_e32 v76, v117, v93
	v_add_f32_e32 v77, v118, v94
	v_mul_f32_e32 v81, 0xbfb8aa3b, v75
	v_exp_f32_e32 v87, v87
	v_fmac_f32_e32 v98, v82, v106
	v_fmac_f32_e32 v97, v90, v113
	s_waitcnt vmcnt(8)
	v_add_f32_e32 v79, v120, v96
	v_mul_f32_e32 v82, 0xbfb8aa3b, v76
	v_mul_f32_e32 v86, 0xbfb8aa3b, v77
	v_exp_f32_e32 v81, v81
	v_add_f32_e32 v80, v121, v97
	v_mul_f32_e32 v88, 0xbfb8aa3b, v79
	v_exp_f32_e32 v82, v82
	v_exp_f32_e32 v86, v86
	v_mul_f32_e32 v89, 0xbfb8aa3b, v80
	v_exp_f32_e32 v88, v88
	v_exp_f32_e32 v89, v89
	v_add_f32_e32 v87, 1.0, v87
	v_add_f32_e32 v81, 1.0, v81
	v_rcp_f32_e32 v87, v87
	v_add_f32_e32 v82, 1.0, v82
	v_add_f32_e32 v86, 1.0, v86
	v_rcp_f32_e32 v81, v81
	v_add_f32_e32 v88, 1.0, v88
	v_rcp_f32_e32 v82, v82
	v_rcp_f32_e32 v86, v86
	v_add_f32_e32 v89, 1.0, v89
	v_rcp_f32_e32 v88, v88
	v_rcp_f32_e32 v89, v89
	v_mul_f32_e32 v78, v78, v87
	v_mul_f32_e32 v75, v75, v81
	v_mul_f32_e32 v87, 0x3e000000, v78
	v_fmac_f32_e32 v98, v85, v114
	v_mul_f32_e32 v78, v99, v131
	v_mul_f32_e32 v76, v76, v82
	v_mul_f32_e32 v77, v77, v86
	v_mul_f32_e32 v81, 0x3e000000, v75
	v_add_f32_e32 v75, v122, v98
	v_fmac_f32_e32 v78, v72, v107
	v_mul_f32_e32 v82, 0x3e000000, v76
	v_mul_f32_e32 v86, 0x3e000000, v77
	v_mul_f32_e32 v76, 0xbfb8aa3b, v75
	v_mul_f32_e32 v77, v79, v88
	v_fmac_f32_e32 v78, v83, v115
	v_exp_f32_e32 v76, v76
	v_mul_f32_e32 v85, 0x3e000000, v77
	v_mul_f32_e32 v77, v80, v89
	v_add_f32_e32 v80, v123, v78
	v_mul_f32_e32 v72, 0xbfb8aa3b, v80
	v_exp_f32_e32 v72, v72
	v_add_f32_e32 v76, 1.0, v76
	v_rcp_f32_e32 v76, v76
	s_waitcnt vmcnt(4)
	v_mul_f32_e32 v26, v26, v130
	v_add_f32_e32 v72, 1.0, v72
	v_rcp_f32_e32 v89, v72
	v_add_co_u32_e32 v72, vcc, s0, v50
	v_fmac_f32_e32 v26, v73, v18
	s_nop 0
	v_addc_co_u32_e32 v73, vcc, 0, v51, vcc
	v_mul_f32_e32 v83, 0x3e000000, v77
	v_mul_f32_e32 v75, v75, v76
	global_load_dwordx4 v[76:79], v[72:73], off offset:1920
	s_waitcnt vmcnt(2)
	v_fmac_f32_e32 v26, v84, v30
	v_add_f32_e32 v22, v22, v26
	v_mul_f32_e32 v18, 0xbfb8aa3b, v22
	v_exp_f32_e32 v26, v18
	v_mul_f32_e32 v18, v27, v129
	v_fmac_f32_e32 v18, v65, v19
	v_fmac_f32_e32 v18, v74, v31
	s_mov_b64 s[0:1], 0x1780
	v_add_f32_e32 v23, v23, v18
	v_lshl_add_u64 v[18:19], v[50:51], 0, s[0:1]
	v_mul_f32_e32 v88, 0x3e000000, v75
	global_load_dwordx4 v[72:75], v[18:19], off offset:16
	v_mul_f32_e32 v10, v10, v126
	v_fmac_f32_e32 v10, v62, v2
	s_waitcnt vmcnt(2)
	v_fmac_f32_e32 v10, v69, v14
	v_add_f32_e32 v2, v6, v10
	v_mul_f32_e32 v6, 0xbfb8aa3b, v2
	v_exp_f32_e32 v6, v6
	v_mul_f32_e32 v11, v11, v125
	v_fmac_f32_e32 v11, v61, v3
	v_fmac_f32_e32 v11, v68, v15
	v_mul_f32_e32 v27, 0xbfb8aa3b, v23
	v_add_f32_e32 v3, v7, v11
	v_exp_f32_e32 v18, v27
	v_add_f32_e32 v6, 1.0, v6
	v_mul_f32_e32 v7, 0xbfb8aa3b, v3
	v_rcp_f32_e32 v6, v6
	v_exp_f32_e32 v7, v7
	v_add_f32_e32 v18, 1.0, v18
	v_rcp_f32_e32 v18, v18
	v_mul_f32_e32 v2, v2, v6
	v_add_f32_e32 v6, 1.0, v7
	v_mul_f32_e32 v7, v12, v124
	v_fmac_f32_e32 v7, v59, v4
	v_fmac_f32_e32 v7, v66, v16
	v_add_f32_e32 v4, v8, v7
	v_mul_f32_e32 v8, v13, v91
	v_mul_f32_e32 v18, v23, v18
	v_mul_f32_e32 v23, v28, v128
	v_mul_f32_e32 v7, 0xbfb8aa3b, v4
	v_fmac_f32_e32 v8, v60, v5
	v_fmac_f32_e32 v23, v64, v20
	v_rcp_f32_e32 v6, v6
	v_exp_f32_e32 v7, v7
	v_fmac_f32_e32 v8, v67, v17
	v_fmac_f32_e32 v23, v71, v32
	v_add_f32_e32 v5, v9, v8
	v_add_f32_e32 v20, v24, v23
	v_mul_f32_e32 v24, v29, v127
	v_mul_f32_e32 v8, 0xbfb8aa3b, v5
	v_fmac_f32_e32 v24, v63, v21
	v_exp_f32_e32 v8, v8
	v_fmac_f32_e32 v24, v70, v33
	v_mul_f32_e32 v3, v3, v6
	v_add_f32_e32 v6, 1.0, v7
	v_add_f32_e32 v21, v25, v24
	v_rcp_f32_e32 v6, v6
	ds_read_b32 v25, v53 offset:35840
	v_add_f32_e32 v7, 1.0, v8
	v_rcp_f32_e32 v7, v7
	v_mul_f32_e32 v4, v4, v6
	v_mul_f32_e32 v24, 0xbfb8aa3b, v21
	v_exp_f32_e32 v24, v24
	v_mul_f32_e32 v5, v5, v7
	v_mul_f32_e32 v23, 0xbfb8aa3b, v20
	v_add_f32_e32 v26, 1.0, v26
	v_add_f32_e32 v24, 1.0, v24
	v_rcp_f32_e32 v24, v24
	v_exp_f32_e32 v23, v23
	v_rcp_f32_e32 v26, v26
	v_mul_f32_e32 v19, v80, v89
	v_mul_f32_e32 v14, v21, v24
	v_mul_f32_e32 v11, 0x3e000000, v14
	v_mul_f32_e32 v19, 0x3e000000, v19
	v_add_f32_e32 v23, 1.0, v23
	v_mul_f32_e32 v22, v22, v26
	v_rcp_f32_e32 v23, v23
	v_mul_f32_e32 v22, 0x3e000000, v22
	v_mul_f32_e32 v2, 0x3e000000, v2
	s_waitcnt vmcnt(1)
	v_lshlrev_b32_e32 v6, 16, v76
	s_waitcnt lgkmcnt(0)
	v_mul_f32_e32 v6, v25, v6
	v_add_u32_e32 v6, 0x8000, v6
	v_and_b32_e32 v7, 0xffff0000, v76
	ds_write_b16_d16_hi v54, v6 offset:17408
	v_add_u32_e32 v6, 0x8000, v82
	ds_write_b16_d16_hi v54, v6 offset:272
	v_mul_f32_e32 v6, v25, v7
	v_add_u32_e32 v6, 0x8000, v6
	v_lshlrev_b32_e32 v8, 16, v77
	ds_write_b16_d16_hi v54, v6 offset:17680
	v_add_u32_e32 v6, 0x8000, v86
	ds_write_b16_d16_hi v54, v6 offset:544
	v_mul_f32_e32 v6, v25, v8
	v_add_u32_e32 v6, 0x8000, v6
	v_and_b32_e32 v9, 0xffff0000, v77
	ds_write_b16_d16_hi v54, v6 offset:17952
	v_add_u32_e32 v6, 0x8000, v87
	ds_write_b16_d16_hi v54, v6 offset:816
	v_mul_f32_e32 v6, v25, v9
	v_add_u32_e32 v6, 0x8000, v6
	v_lshlrev_b32_e32 v12, 16, v78
	ds_write_b16_d16_hi v54, v6 offset:18224
	v_add_u32_e32 v6, 0x8000, v85
	ds_write_b16_d16_hi v54, v6 offset:1088
	v_mul_f32_e32 v6, v25, v12
	v_add_u32_e32 v6, 0x8000, v6
	v_and_b32_e32 v13, 0xffff0000, v78
	ds_write_b16_d16_hi v54, v6 offset:18496
	v_add_u32_e32 v6, 0x8000, v83
	ds_write_b16_d16_hi v54, v6 offset:1360
	v_mul_f32_e32 v6, v25, v13
	v_add_u32_e32 v6, 0x8000, v6
	v_lshlrev_b32_e32 v14, 16, v79
	ds_write_b16_d16_hi v54, v6 offset:18768
	v_add_u32_e32 v6, 0x8000, v88
	ds_write_b16_d16_hi v54, v6 offset:1632
	v_mul_f32_e32 v6, v25, v14
	v_add_u32_e32 v6, 0x8000, v6
	v_and_b32_e32 v15, 0xffff0000, v79
	ds_write_b16_d16_hi v54, v6 offset:19040
	v_add_u32_e32 v6, 0x8000, v19
	ds_write_b16_d16_hi v54, v6 offset:1904
	v_mul_f32_e32 v6, v25, v15
	v_add_u32_e32 v6, 0x8000, v6
	s_waitcnt vmcnt(0)
	v_lshlrev_b32_e32 v16, 16, v72
	ds_write_b16_d16_hi v54, v6 offset:19312
	v_add_u32_e32 v6, 0x8000, v22
	ds_write_b16_d16_hi v54, v6 offset:2176
	v_mul_f32_e32 v6, v25, v16
	v_mul_f32_e32 v18, 0x3e000000, v18
	v_mul_f32_e32 v10, v20, v23
	v_lshlrev_b32_e32 v23, 16, v74
	v_add_u32_e32 v6, 0x8000, v6
	v_add_u32_e32 v2, 0x8000, v2
	v_and_b32_e32 v17, 0xffff0000, v72
	ds_write_b16_d16_hi v54, v6 offset:19584
	v_add_u32_e32 v6, 0x8000, v18
	ds_write_b16_d16_hi v54, v2 offset:3264
	v_mul_f32_e32 v2, v25, v23
	v_mul_f32_e32 v3, 0x3e000000, v3
	ds_write_b16_d16_hi v54, v6 offset:2448
	v_mul_f32_e32 v6, v25, v17
	v_add_u32_e32 v2, 0x8000, v2
	v_mul_f32_e32 v10, 0x3e000000, v10
	v_and_b32_e32 v24, 0xffff0000, v74
	v_add_u32_e32 v6, 0x8000, v6
	ds_write_b16_d16_hi v54, v2 offset:20672
	v_add_u32_e32 v2, 0x8000, v3
	v_lshlrev_b32_e32 v20, 16, v73
	ds_write_b16_d16_hi v54, v6 offset:19856
	v_add_u32_e32 v6, 0x8000, v10
	ds_write_b16_d16_hi v54, v2 offset:3536
	v_mul_f32_e32 v2, v25, v24
	v_mul_f32_e32 v4, 0x3e000000, v4
	ds_write_b16_d16_hi v54, v6 offset:2720
	v_mul_f32_e32 v6, v25, v20
	v_add_u32_e32 v2, 0x8000, v2
	v_lshlrev_b32_e32 v26, 16, v75
	v_add_u32_e32 v6, 0x8000, v6
	ds_write_b16_d16_hi v54, v2 offset:20944
	v_add_u32_e32 v2, 0x8000, v4
	v_and_b32_e32 v21, 0xffff0000, v73
	ds_write_b16_d16_hi v54, v6 offset:20128
	v_add_u32_e32 v6, 0x8000, v11
	ds_write_b16_d16_hi v54, v2 offset:3808
	v_mul_f32_e32 v2, v25, v26
	v_mul_f32_e32 v5, 0x3e000000, v5
	ds_write_b16_d16_hi v54, v6 offset:2992
	v_mul_f32_e32 v6, v25, v21
	v_add_u32_e32 v2, 0x8000, v2
	v_and_b32_e32 v27, 0xffff0000, v75
	v_add_u32_e32 v28, 0x8000, v81
	v_add_u32_e32 v6, 0x8000, v6
	ds_write_b16_d16_hi v54, v2 offset:21216
	v_add_u32_e32 v2, 0x8000, v5
	ds_write_b16_d16_hi v54, v28
	ds_write_b16_d16_hi v54, v6 offset:20400
	ds_write_b16_d16_hi v55, v2
	v_mul_f32_e32 v2, v25, v27
	v_add_u32_e32 v2, 0x8000, v2
	ds_write_b16_d16_hi v55, v2 offset:17408
	s_waitcnt lgkmcnt(0)
	s_barrier
	ds_read_b128 v[2:5], v38 offset:17408
	ds_read_b128 v[6:9], v58
	ds_read_b128 v[10:13], v38 offset:17472
	ds_read_b128 v[14:17], v58 offset:64
	s_waitcnt lgkmcnt(2)
	v_mfma_f32_16x16x32_bf16 v[6:9], v[2:5], v[6:9], 0
	ds_read_b128 v[18:21], v58 offset:4352
	ds_read_b128 v[22:25], v58 offset:4416
	s_mul_hi_i32 s1, s9, 34
	s_add_u32 s0, s8, s10
	s_waitcnt lgkmcnt(2)
	v_mfma_f32_16x16x32_bf16 v[6:9], v[10:13], v[14:17], v[6:9]
	ds_read_b128 v[14:17], v38 offset:17536
	s_addc_u32 s1, s1, s4
	s_lshl_b64 s[8:9], s[0:1], 14
	s_waitcnt lgkmcnt(2)
	v_mfma_f32_16x16x32_bf16 v[2:5], v[2:5], v[18:21], 0
	v_readlane_b32 s10, v253, 29
	v_readlane_b32 s11, v253, 30
	s_add_u32 s8, s10, s8
	s_waitcnt lgkmcnt(1)
	v_mfma_f32_16x16x32_bf16 v[2:5], v[10:13], v[22:25], v[2:5]
	ds_read_b128 v[10:13], v58 offset:128
	ds_read_b128 v[18:21], v38 offset:17600
	ds_read_b128 v[22:25], v58 offset:192
	s_addc_u32 s9, s11, s9
	s_waitcnt lgkmcnt(2)
	v_mfma_f32_16x16x32_bf16 v[6:9], v[14:17], v[10:13], v[6:9]
	ds_read_b128 v[10:13], v58 offset:4480
	ds_read_b128 v[26:29], v58 offset:4544
	s_waitcnt lgkmcnt(1)
	v_mfma_f32_16x16x32_bf16 v[2:5], v[14:17], v[10:13], v[2:5]
	v_lshl_add_u64 v[10:11], v[42:43], 2, s[8:9]
	v_mfma_f32_16x16x32_bf16 v[6:9], v[18:21], v[22:25], v[6:9]
	s_waitcnt lgkmcnt(0)
	v_mfma_f32_16x16x32_bf16 v[2:5], v[18:21], v[26:29], v[2:5]
	s_nop 5
	global_store_dword v[10:11], v6, off
	v_lshl_add_u64 v[10:11], v[40:41], 2, s[8:9]
	global_store_dword v[10:11], v7, off offset:256
	global_store_dword v[10:11], v8, off offset:512
	global_store_dword v[10:11], v9, off offset:768
	global_store_dword v[10:11], v2, off offset:64
	v_lshl_add_u64 v[6:7], v[48:49], 2, s[8:9]
	global_store_dword v[6:7], v3, off offset:256
	global_store_dword v[6:7], v4, off offset:512
	global_store_dword v[6:7], v5, off offset:768
	s_and_saveexec_b64 s[8:9], s[44:45]
	s_cbranch_execnz .LBB0_744
	s_or_b64 exec, exec, s[8:9]
	s_and_saveexec_b64 s[0:1], s[40:41]
	s_cbranch_execz .LBB0_727
	s_branch .LBB0_747
	s_nop 0
	s_nop 0
	s_nop 0
	s_nop 0
	s_nop 0
	s_nop 0
	s_nop 0
	s_nop 0
	s_nop 0
	s_nop 0
	s_nop 0
	s_nop 0
	s_nop 0
	s_nop 0
	s_nop 0
	s_nop 0
	s_nop 0
	s_nop 0
	s_nop 0
	s_nop 0
	s_nop 0
	s_nop 0
	s_nop 0
	s_nop 0
	s_nop 0
	s_nop 0
	s_nop 0
	s_nop 0
	s_nop 0
	s_nop 0
	s_nop 0
	s_nop 0
	s_nop 0
	s_nop 0
	s_nop 0
	s_nop 0
	s_nop 0
	s_nop 0
	s_nop 0
	s_nop 0
	s_nop 0
	s_nop 0
	s_nop 0
	s_nop 0
	s_nop 0
	s_nop 0
	s_nop 0
	s_nop 0
	s_nop 0
	s_nop 0
	s_nop 0
	s_nop 0
	s_nop 0
	s_nop 0
	s_nop 0
	s_nop 0
	s_nop 0
	s_nop 0
	s_nop 0
	s_nop 0
	s_nop 0
	s_nop 0
	s_nop 0
	s_nop 0
	s_nop 0
	s_nop 0
	s_nop 0
	s_nop 0
	s_nop 0
	s_nop 0
	s_nop 0
	s_nop 0
	s_nop 0
	s_nop 0
	s_nop 0
	s_nop 0
	s_nop 0
	s_nop 0
	s_nop 0
	s_nop 0
	s_nop 0
	s_nop 0
	s_nop 0
	s_nop 0
	s_nop 0
	s_nop 0
	s_nop 0
	s_nop 0
	s_nop 0
	s_nop 0
	s_nop 0
	s_nop 0
	s_nop 0
	s_nop 0
	s_nop 0
	s_nop 0
	s_nop 0
	s_nop 0
	s_nop 0
	s_nop 0
	s_nop 0
	s_nop 0
	s_nop 0
	s_nop 0
	s_nop 0
	s_nop 0
	s_nop 0
	s_nop 0
	s_nop 0
	s_nop 0
	s_nop 0
	s_nop 0
